# v56: v54 + first-tile expert lookups at MoE up/down phase starts read from the LDS table
# speedup vs baseline: 1.0034x; 1.0016x over previous
.LBB0_1479:
	s_cmp_lt_i32 s48, 0
	s_cselect_b64 s[14:15], -1, 0
	s_ashr_i32 s13, s12, 31
	s_lshr_b32 s3, s13, 29
	s_add_i32 s3, s12, s3
	s_ashr_i32 s49, s3, 3
	s_and_b32 s3, s3, -8
	s_sub_i32 s50, s12, s3
	s_add_i32 s51, s49, 1
	s_cmp_lg_u64 s[10:11], 0
	s_cselect_b64 s[16:17], -1, 0
	s_ashr_i32 s3, s2, 31
	s_cmp_gt_i32 s48, -1
	s_mul_i32 s52, s51, s50
	s_mov_b64 s[22:23], -1
	s_mov_b32 s38, s2
	s_mov_b32 s36, s48
	s_mov_b64 s[6:7], s[2:3]
	s_waitcnt vmcnt(0)
	v_mbcnt_lo_u32_b32 v0, -1, 0
	v_mbcnt_hi_u32_b32 v0, -1, v0
	s_cbranch_scc1 .LBB0_1486
	s_cmp_lt_i32 s2, s12
	s_cbranch_scc0 .LBB0_1484
	s_lshr_b32 s6, s3, 29
	s_add_i32 s6, s2, s6
	s_ashr_i32 s7, s6, 3
	s_and_b32 s6, s6, -8
	s_sub_i32 s6, s2, s6
	s_sub_i32 s22, s6, s50
	s_mul_i32 s22, s22, s49
	s_add_i32 s22, s22, s52
	s_cmp_lt_i32 s6, s50
	s_mul_i32 s6, s6, s51
	s_cselect_b32 s6, s6, s22
	s_add_i32 s6, s6, s7
	s_mul_hi_i32 s7, s6, 0x2e8ba2e9
	s_lshr_b32 s22, s7, 31
	s_ashr_i32 s7, s7, 5
	s_add_i32 s7, s7, s22
	s_lshl_b32 s22, s7, 3
	s_sub_i32 s23, s5, s22
	s_min_i32 s23, s23, 8
	s_abs_i32 s29, s23
	v_cvt_f32_u32_e32 v2, s29
	s_sub_i32 s31, 0, s29
	s_mulk_i32 s7, 0xb0
	s_sub_i32 s6, s6, s7
	v_rcp_iflag_f32_e32 v2, v2
	s_abs_i32 s30, s6
	s_xor_b32 s7, s6, s23
	s_ashr_i32 s7, s7, 31
	v_mul_f32_e32 v2, 0x4f7ffffe, v2
	v_cvt_u32_f32_e32 v2, v2
	s_nop 0
	v_readfirstlane_b32 s34, v2
	s_mul_i32 s31, s31, s34
	s_mul_hi_u32 s31, s34, s31
	s_add_i32 s34, s34, s31
	s_mul_hi_u32 s31, s30, s34
	s_mul_i32 s34, s31, s29
	s_sub_i32 s30, s30, s34
	s_add_i32 s34, s31, 1
	s_sub_i32 s35, s30, s29
	s_cmp_ge_u32 s30, s29
	s_cselect_b32 s31, s34, s31
	s_cselect_b32 s30, s35, s30
	s_add_i32 s34, s31, 1
	s_cmp_ge_u32 s30, s29
	s_cselect_b32 s29, s34, s31
	s_xor_b32 s29, s29, s7
	s_sub_i32 s36, s29, s7
	s_mul_i32 s7, s36, s23
	s_sub_i32 s6, s6, s7
	s_add_i32 s38, s22, s6
	s_andn2_b64 vcc, exec, s[16:17]
	s_ashr_i32 s39, s38, 31
	s_cbranch_vccnz .LBB0_1483
	s_lshl_b32 s6, s38, 2
	s_add_i32 s6, s6, 0x21000
	v_mov_b32_e32 v2, s6
	ds_read_b32 v2, v2
	s_waitcnt lgkmcnt(0)
	v_readfirstlane_b32 s65, v2

.LBB0_1620:
	s_andn2_b64 vcc, exec, s[6:7]
	s_cbranch_vccnz .LBB0_1677
	s_cmp_lt_i32 s40, 0
	s_cselect_b64 s[16:17], -1, 0
	s_ashr_i32 s11, s10, 31
	s_lshr_b32 s3, s11, 29
	s_add_i32 s3, s10, s3
	s_ashr_i32 s45, s3, 3
	s_and_b32 s3, s3, -8
	s_sub_i32 s47, s10, s3
	s_add_i32 s48, s45, 1
	s_cmp_lg_u64 s[4:5], 0
	s_cselect_b64 s[18:19], -1, 0
	s_ashr_i32 s3, s2, 31
	s_mov_b64 s[6:7], 0
	s_cmp_gt_i32 s40, -1
	s_mul_i32 s49, s48, s47
	s_mov_b64 s[20:21], -1
	s_mov_b32 s30, s2
	s_mov_b32 s57, s40
	s_mov_b64 s[8:9], s[2:3]
	v_mbcnt_lo_u32_b32 v0, -1, 0
	v_mbcnt_hi_u32_b32 v0, -1, v0
	s_cbranch_scc1 .LBB0_1646
	s_cmp_lt_i32 s2, s10
	s_cbranch_scc0 .LBB0_1625
	s_lshr_b32 s6, s3, 29
	s_add_i32 s6, s2, s6
	s_ashr_i32 s7, s6, 3
	s_and_b32 s6, s6, -8
	s_sub_i32 s6, s2, s6
	s_sub_i32 s8, s6, s47
	s_mul_i32 s8, s8, s45
	s_add_i32 s8, s8, s49
	s_cmp_lt_i32 s6, s47
	s_mul_i32 s6, s48, s6
	s_cselect_b32 s6, s6, s8
	s_add_i32 s6, s6, s7
	s_ashr_i32 s7, s6, 31
	s_lshr_b32 s7, s7, 27
	s_add_i32 s7, s6, s7
	s_ashr_i32 s8, s7, 5
	s_lshl_b32 s8, s8, 3
	s_sub_i32 s9, s13, s8
	s_min_i32 s9, s9, 8
	s_abs_i32 s20, s9
	v_cvt_f32_u32_e32 v2, s20
	s_sub_i32 s22, 0, s20
	s_andn2_b32 s7, s7, 31
	s_sub_i32 s6, s6, s7
	v_rcp_iflag_f32_e32 v2, v2
	s_abs_i32 s7, s6
	s_xor_b32 s21, s6, s9
	s_ashr_i32 s21, s21, 31
	v_mul_f32_e32 v2, 0x4f7ffffe, v2
	v_cvt_u32_f32_e32 v2, v2
	s_nop 0
	v_readfirstlane_b32 s23, v2
	s_mul_i32 s22, s22, s23
	s_mul_hi_u32 s22, s23, s22
	s_add_i32 s23, s23, s22
	s_mul_hi_u32 s22, s7, s23
	s_mul_i32 s23, s22, s20
	s_sub_i32 s7, s7, s23
	s_add_i32 s26, s22, 1
	s_sub_i32 s23, s7, s20
	s_cmp_ge_u32 s7, s20
	s_cselect_b32 s22, s26, s22
	s_cselect_b32 s7, s23, s7
	s_add_i32 s23, s22, 1
	s_cmp_ge_u32 s7, s20
	s_cselect_b32 s7, s23, s22
	s_xor_b32 s7, s7, s21
	s_sub_i32 s57, s7, s21
	s_mul_i32 s7, s57, s9
	s_sub_i32 s6, s6, s7
	s_add_i32 s30, s8, s6
	s_andn2_b64 vcc, exec, s[18:19]
	s_ashr_i32 s31, s30, 31
	s_cbranch_vccnz .LBB0_1643
	s_lshl_b32 s6, s30, 2
	s_add_i32 s6, s6, 0x21000
	v_mov_b32_e32 v2, s6
	ds_read_b32 v2, v2
	s_waitcnt lgkmcnt(0)
	v_readfirstlane_b32 s6, v2
	s_mul_hi_i32 s7, s6, 0x2c0000
	s_mul_i32 s6, s6, 0x2c0000
	s_branch .LBB0_1644
